# grid barrier, leader exit path: the acquire invalidate is issued without first waiting for the release atomic's acknowledgement (one wait for both)
# baseline (speedup 1.0000x reference)
; __device__ __forceinline__ unsigned xb_add(unsigned* p, unsigned v) { return __hip_atomic_fetch_add(p, v, __ATOMIC_RELAXED, __HIP_MEMORY_SCOPE_AGENT); }
; __device__ __forceinline__ void xcd_barrier(const XcdBarrier& b) {
;     ...
;             __builtin_amdgcn_fence(__ATOMIC_ACQUIRE, "agent");
;             xb_add(&bar[XB_XGEN(b.x)], 1u);
;             asm volatile("s_waitcnt vmcnt(0)" ::: "memory");
.LBB0_160:
	s_or_b64 exec, exec, s[8:9]
	s_mov_b64 s[8:9], exec
	v_mbcnt_lo_u32_b32 v1, s8, 0
	v_mbcnt_hi_u32_b32 v1, s9, v1
	v_cmp_eq_u32_e32 vcc, 0, v1
	buffer_inv sc1
	s_and_saveexec_b64 s[10:11], vcc
	s_cbranch_execz .LBB0_162
	s_bcnt1_i32_b64 s3, s[8:9]
	v_mov_b32_e32 v1, 0x2000
	v_mov_b32_e32 v2, s3

; __device__ __forceinline__ unsigned xb_add(unsigned* p, unsigned v) { return __hip_atomic_fetch_add(p, v, __ATOMIC_RELAXED, __HIP_MEMORY_SCOPE_AGENT); }
; __device__ __forceinline__ void xcd_barrier(const XcdBarrier& b) {
;     ...
;             __builtin_amdgcn_fence(__ATOMIC_ACQUIRE, "agent");
;             xb_add(&bar[XB_XGEN(b.x)], 1u);
;             asm volatile("s_waitcnt vmcnt(0)" ::: "memory");
.LBB0_312:
	s_or_b64 exec, exec, s[8:9]
	s_mov_b64 s[8:9], exec
	v_mbcnt_lo_u32_b32 v1, s8, 0
	v_mbcnt_hi_u32_b32 v1, s9, v1
	v_cmp_eq_u32_e32 vcc, 0, v1
	buffer_inv sc1
	s_and_saveexec_b64 s[10:11], vcc
	s_cbranch_execz .LBB0_314
	s_bcnt1_i32_b64 s3, s[8:9]
	v_mov_b32_e32 v1, s3
	v_mov_b32_e32 v2, 0x2000

; __device__ __forceinline__ unsigned xb_add(unsigned* p, unsigned v) { return __hip_atomic_fetch_add(p, v, __ATOMIC_RELAXED, __HIP_MEMORY_SCOPE_AGENT); }
; __device__ __forceinline__ void xcd_barrier(const XcdBarrier& b) {
;     ...
;             __builtin_amdgcn_fence(__ATOMIC_ACQUIRE, "agent");
;             xb_add(&bar[XB_XGEN(b.x)], 1u);
;             asm volatile("s_waitcnt vmcnt(0)" ::: "memory");
.LBB0_467:
	s_or_b64 exec, exec, s[8:9]
	s_mov_b64 s[8:9], exec
	v_mbcnt_lo_u32_b32 v2, s8, 0
	v_mbcnt_hi_u32_b32 v2, s9, v2
	v_cmp_eq_u32_e32 vcc, 0, v2
	buffer_inv sc1
	s_and_saveexec_b64 s[10:11], vcc
	s_cbranch_execz .LBB0_469
	s_bcnt1_i32_b64 s8, s[8:9]
	v_mov_b32_e32 v2, s8
	v_mov_b32_e32 v3, 0x2000

; __device__ __forceinline__ unsigned xb_add(unsigned* p, unsigned v) { return __hip_atomic_fetch_add(p, v, __ATOMIC_RELAXED, __HIP_MEMORY_SCOPE_AGENT); }
; __device__ __forceinline__ void xcd_barrier(const XcdBarrier& b) {
;     ...
;             __builtin_amdgcn_fence(__ATOMIC_ACQUIRE, "agent");
;             xb_add(&bar[XB_XGEN(b.x)], 1u);
;             asm volatile("s_waitcnt vmcnt(0)" ::: "memory");
.LBB0_571:
	s_or_b64 exec, exec, s[14:15]
	s_mov_b64 s[14:15], exec
	v_mbcnt_lo_u32_b32 v2, s14, 0
	v_mbcnt_hi_u32_b32 v2, s15, v2
	v_cmp_eq_u32_e32 vcc, 0, v2
	buffer_inv sc1
	s_and_saveexec_b64 s[24:25], vcc
	s_cbranch_execz .LBB0_573
	s_bcnt1_i32_b64 s14, s[14:15]
	v_mov_b32_e32 v2, s14
	v_mov_b32_e32 v3, 0x2000

; __device__ __forceinline__ unsigned xb_add(unsigned* p, unsigned v) { return __hip_atomic_fetch_add(p, v, __ATOMIC_RELAXED, __HIP_MEMORY_SCOPE_AGENT); }
; __device__ __forceinline__ void xcd_barrier(const XcdBarrier& b) {
;     ...
;             __builtin_amdgcn_fence(__ATOMIC_ACQUIRE, "agent");
;             xb_add(&bar[XB_XGEN(b.x)], 1u);
;             asm volatile("s_waitcnt vmcnt(0)" ::: "memory");
.LBB0_805:
	s_or_b64 exec, exec, s[8:9]
	s_mov_b64 s[8:9], exec
	v_mbcnt_lo_u32_b32 v1, s8, 0
	v_mbcnt_hi_u32_b32 v1, s9, v1
	v_cmp_eq_u32_e32 vcc, 0, v1
	buffer_inv sc1
	s_and_saveexec_b64 s[14:15], vcc
	s_cbranch_execz .LBB0_807
	s_bcnt1_i32_b64 s3, s[8:9]
	v_mov_b32_e32 v1, s3
	v_mov_b32_e32 v2, 0x2000

; __device__ __forceinline__ unsigned xb_add(unsigned* p, unsigned v) { return __hip_atomic_fetch_add(p, v, __ATOMIC_RELAXED, __HIP_MEMORY_SCOPE_AGENT); }
; __device__ __forceinline__ void xcd_barrier(const XcdBarrier& b) {
;     ...
;             __builtin_amdgcn_fence(__ATOMIC_ACQUIRE, "agent");
;             xb_add(&bar[XB_XGEN(b.x)], 1u);
;             asm volatile("s_waitcnt vmcnt(0)" ::: "memory");
.LBB0_1110:
	s_or_b64 exec, exec, s[8:9]
	s_mov_b64 s[8:9], exec
	v_mbcnt_lo_u32_b32 v2, s8, 0
	v_mbcnt_hi_u32_b32 v2, s9, v2
	v_cmp_eq_u32_e32 vcc, 0, v2
	buffer_inv sc1
	s_and_saveexec_b64 s[10:11], vcc
	s_cbranch_execz .LBB0_1112
	s_bcnt1_i32_b64 s2, s[8:9]
	v_mov_b32_e32 v2, s2
	v_mov_b32_e32 v3, 0x2000

; __device__ __forceinline__ unsigned xb_add(unsigned* p, unsigned v) { return __hip_atomic_fetch_add(p, v, __ATOMIC_RELAXED, __HIP_MEMORY_SCOPE_AGENT); }
; __device__ __forceinline__ void xcd_barrier(const XcdBarrier& b) {
;     ...
;             __builtin_amdgcn_fence(__ATOMIC_ACQUIRE, "agent");
;             xb_add(&bar[XB_XGEN(b.x)], 1u);
;             asm volatile("s_waitcnt vmcnt(0)" ::: "memory");
.LBB0_1458:
	s_or_b64 exec, exec, s[8:9]
	s_mov_b64 s[8:9], exec
	v_mbcnt_lo_u32_b32 v1, s8, 0
	v_mbcnt_hi_u32_b32 v1, s9, v1
	v_cmp_eq_u32_e32 vcc, 0, v1
	buffer_inv sc1
	s_and_saveexec_b64 s[10:11], vcc
	s_cbranch_execz .LBB0_1460
	s_bcnt1_i32_b64 s8, s[8:9]
	v_mov_b32_e32 v1, s8
	v_mov_b32_e32 v2, 0x2000

; __device__ __forceinline__ unsigned xb_add(unsigned* p, unsigned v) { return __hip_atomic_fetch_add(p, v, __ATOMIC_RELAXED, __HIP_MEMORY_SCOPE_AGENT); }
; __device__ __forceinline__ void xcd_barrier(const XcdBarrier& b) {
;     ...
;             __builtin_amdgcn_fence(__ATOMIC_ACQUIRE, "agent");
;             xb_add(&bar[XB_XGEN(b.x)], 1u);
;             asm volatile("s_waitcnt vmcnt(0)" ::: "memory");
.LBB0_1534:
	s_or_b64 exec, exec, s[8:9]
	s_mov_b64 s[8:9], exec
	v_mbcnt_lo_u32_b32 v1, s8, 0
	v_mbcnt_hi_u32_b32 v1, s9, v1
	v_cmp_eq_u32_e32 vcc, 0, v1
	buffer_inv sc1
	s_and_saveexec_b64 s[10:11], vcc
	s_cbranch_execnz .LBB0_1535
	s_getpc_b64 s[98:99]
